# batch the 16 barrier-census loads; batch LDS reads in x1 un-sum loop
# baseline (speedup 1.0000x reference)
; __device__ __forceinline__ unsigned xb_ld(unsigned* p)              { return __hip_atomic_load(p, __ATOMIC_RELAXED, __HIP_MEMORY_SCOPE_AGENT); }
; __device__ __forceinline__ void xcd_barrier_complete(unsigned* bar, unsigned x, unsigned& nloc, unsigned& nx) {
;     ...
;     for (;;) {
;         sum = 0u; cnt = 0u; mine = 0u;
; #pragma unroll
;         for (unsigned j = 0; j < 16; ++j) { const unsigned c = xb_ld(&bar[XB_XCNT(j)]); sum += c; cnt += (c > 0u) ? 1u : 0u; mine = (j == x) ? c : mine; }
;         if (sum == G) break;
;         __builtin_amdgcn_s_sleep(1);
;         if ((++sp & 255u) == 0u) { if (xb_ld(&bar[XB_TMO])) break; if (sp > XB_SPIN_CAP) { atomicAdd(&bar[XB_TMO], 1u); break; } }
;     }
.LBB0_52:
	v_readlane_b32 s2, v252, 16
	v_readlane_b32 s3, v252, 17
	s_mov_b64 s[14:15], -1
	s_nop 4
	global_load_dword v0, v97, s[2:3] sc1
	v_readlane_b32 s2, v252, 18
	v_readlane_b32 s3, v252, 19
	s_nop 4
	global_load_dword v1, v97, s[2:3] sc1
	v_readlane_b32 s2, v252, 20
	v_readlane_b32 s3, v252, 21
	s_nop 4
	global_load_dword v2, v97, s[2:3] sc1
	v_readlane_b32 s2, v252, 22
	v_readlane_b32 s3, v252, 23
	s_nop 4
	global_load_dword v3, v97, s[2:3] sc1
	v_readlane_b32 s2, v252, 24
	v_readlane_b32 s3, v252, 25
	s_nop 4
	global_load_dword v4, v97, s[2:3] sc1
	v_readlane_b32 s2, v252, 26
	v_readlane_b32 s3, v252, 27
	s_nop 4
	global_load_dword v5, v97, s[2:3] sc1
	v_readlane_b32 s2, v252, 28
	v_readlane_b32 s3, v252, 29
	s_nop 4
	global_load_dword v6, v97, s[2:3] sc1
	v_readlane_b32 s2, v252, 30
	v_readlane_b32 s3, v252, 31
	s_nop 4
	global_load_dword v7, v97, s[2:3] sc1
	v_readlane_b32 s2, v252, 32
	v_readlane_b32 s3, v252, 33
	s_nop 4
	global_load_dword v8, v97, s[2:3] sc1
	v_readlane_b32 s2, v252, 34
	v_readlane_b32 s3, v252, 35
	s_nop 4
	global_load_dword v9, v97, s[2:3] sc1
	v_readlane_b32 s2, v252, 36
	v_readlane_b32 s3, v252, 37
	s_nop 4
	global_load_dword v10, v97, s[2:3] sc1
	v_readlane_b32 s2, v252, 38
	v_readlane_b32 s3, v252, 39
	s_nop 4
	global_load_dword v11, v97, s[2:3] sc1
	v_readlane_b32 s2, v252, 40
	v_readlane_b32 s3, v252, 41
	s_nop 4
	global_load_dword v12, v97, s[2:3] sc1
	v_readlane_b32 s2, v252, 42
	v_readlane_b32 s3, v252, 43
	s_nop 4
	global_load_dword v13, v97, s[2:3] sc1
	v_readlane_b32 s2, v252, 44
	v_readlane_b32 s3, v252, 45
	s_nop 4
	global_load_dword v14, v97, s[2:3] sc1
	v_readlane_b32 s2, v252, 46
	v_readlane_b32 s3, v252, 47
	s_nop 4
	global_load_dword v15, v97, s[2:3] sc1
	s_mov_b64 s[2:3], -1
	s_waitcnt vmcnt(0)
	v_add_u32_e32 v16, v1, v0
	v_add_u32_e32 v16, v16, v2
	v_add_u32_e32 v16, v16, v3
	v_add_u32_e32 v16, v16, v4
	v_add_u32_e32 v16, v16, v5
	v_add_u32_e32 v16, v16, v6
	v_add_u32_e32 v16, v16, v7
	v_add_u32_e32 v16, v16, v8
	v_add_u32_e32 v16, v16, v9
	v_add_u32_e32 v16, v16, v10
	v_add_u32_e32 v16, v16, v11
	v_add_u32_e32 v16, v16, v12
	v_add_u32_e32 v16, v16, v13
	v_add_u32_e32 v16, v16, v14
	v_add_u32_e32 v16, v16, v15
	v_cmp_eq_u32_e32 vcc, s4, v16
	s_cbranch_vccnz .LBB0_51
	s_and_b32 s2, s5, 0xff
	s_cmp_eq_u32 s2, 0
	s_mov_b64 s[2:3], -1
	s_mov_b64 s[20:21], -1
	s_sleep 1
	s_cbranch_scc0 .LBB0_56
	global_load_dword v16, v97, s[82:83] sc1
	s_waitcnt vmcnt(0)
	v_cmp_eq_u32_e32 vcc, 0, v16
	s_cbranch_vccnz .LBB0_58
	s_mov_b64 s[20:21], 0

; __device__ __forceinline__ void x1_wave(int item, int b0, const h16* __restrict__ proj, const float* __restrict__ small, const float* __restrict__ convw, ...
;     ...
;     {   float sum = 0.f;
;         lds_cptr kp = (lds_cptr)(R + W_K) + (lane >> 5) * 4096 + (lane & 31) * 2;
; #pragma unroll 16
;         for (int q = 0; q < 64; ++q) sum += (float)*(const __attribute__((address_space(3))) h16*)(kp + q * 64);
;         un[((size_t)gbh * 32 + c) * 64 + lane] = sum; }
.LBB0_919:
	v_add_u32_e32 v2, s0, v0
	ds_read_u16 v4, v2
	ds_read_u16 v5, v2 offset:64
	ds_read_u16 v6, v2 offset:128
	ds_read_u16 v7, v2 offset:192
	ds_read_u16 v8, v2 offset:256
	ds_read_u16 v9, v2 offset:320
	ds_read_u16 v10, v2 offset:384
	ds_read_u16 v11, v2 offset:448
	ds_read_u16 v12, v2 offset:512
	ds_read_u16 v13, v2 offset:576
	ds_read_u16 v14, v2 offset:640
	ds_read_u16 v15, v2 offset:704
	ds_read_u16 v16, v2 offset:768
	ds_read_u16 v17, v2 offset:832
	ds_read_u16 v18, v2 offset:896
	ds_read_u16 v19, v2 offset:960
	s_addk_i32 s0, 0x400
	s_cmpk_lg_i32 s0, 0x1000
	s_waitcnt lgkmcnt(14)
	v_cvt_f32_f16_e32 v4, v4
	v_add_f32_e32 v1, v1, v4
	s_waitcnt lgkmcnt(13)
	v_cvt_f32_f16_e32 v5, v5
	v_add_f32_e32 v1, v1, v5
	s_waitcnt lgkmcnt(12)
	v_cvt_f32_f16_e32 v6, v6
	v_add_f32_e32 v1, v1, v6
	s_waitcnt lgkmcnt(11)
	v_cvt_f32_f16_e32 v7, v7
	v_add_f32_e32 v1, v1, v7
	s_waitcnt lgkmcnt(10)
	v_cvt_f32_f16_e32 v8, v8
	v_add_f32_e32 v1, v1, v8
	s_waitcnt lgkmcnt(9)
	v_cvt_f32_f16_e32 v9, v9
	v_add_f32_e32 v1, v1, v9
	s_waitcnt lgkmcnt(8)
	v_cvt_f32_f16_e32 v10, v10
	v_add_f32_e32 v1, v1, v10
	s_waitcnt lgkmcnt(7)
	v_cvt_f32_f16_e32 v11, v11
	v_add_f32_e32 v1, v1, v11
	s_waitcnt lgkmcnt(6)
	v_cvt_f32_f16_e32 v12, v12
	v_add_f32_e32 v1, v1, v12
	s_waitcnt lgkmcnt(5)
	v_cvt_f32_f16_e32 v13, v13
	v_add_f32_e32 v1, v1, v13
	s_waitcnt lgkmcnt(4)
	v_cvt_f32_f16_e32 v14, v14
	v_add_f32_e32 v1, v1, v14
	s_waitcnt lgkmcnt(3)
	v_cvt_f32_f16_e32 v15, v15
	v_add_f32_e32 v1, v1, v15
	s_waitcnt lgkmcnt(2)
	v_cvt_f32_f16_e32 v16, v16
	v_add_f32_e32 v1, v1, v16
	s_waitcnt lgkmcnt(1)
	v_cvt_f32_f16_e32 v17, v17
	v_add_f32_e32 v1, v1, v17
	s_waitcnt lgkmcnt(0)
	v_cvt_f32_f16_e32 v18, v18
	v_add_f32_e32 v1, v1, v18
	s_waitcnt lgkmcnt(0)
	v_cvt_f32_f16_e32 v19, v19
	v_add_f32_e32 v1, v1, v19
	s_cbranch_scc1 .LBB0_919
	s_ashr_i32 s15, s14, 31
	s_lshl_b64 s[0:1], s[14:15], 13
	v_readlane_b32 s14, v254, 30
	v_readlane_b32 s15, v254, 31
	s_add_u32 s0, s14, s0
	s_addc_u32 s1, s15, s1
	s_lshl_b32 s12, s12, 8
	s_add_u32 s0, s0, s12
	s_addc_u32 s1, s1, 0
	v_lshl_add_u64 v[2:3], v[174:175], 2, s[0:1]
	global_store_dword v[2:3], v1, off
	v_readlane_b32 s0, v252, 14
	s_waitcnt lgkmcnt(0)
	v_readlane_b32 s1, v252, 15
	s_load_dword s0, s[0:1], 0x0
	s_waitcnt lgkmcnt(0)
	s_lshl_b32 s0, s0, 2
	s_add_i32 s6, s0, s6
	s_cmpk_lt_i32 s6, 0x400
	s_cbranch_scc1 .LBB0_882
	v_readlane_b32 s45, v255, 35
	s_mov_b64 s[62:63], 0x80
